# v045 with s_sleep 8 instead of s_sleep 1 between polls of the barrier arrival counter (fewer polls on the hot address)
# speedup vs baseline: 1.0082x; 1.0015x over previous
.LBB0_184:
	s_and_b32 s16, s23, 0xff
	s_mov_b64 s[14:15], -1
	s_cmp_lg_u32 s16, 0
	s_mov_b64 s[24:25], -1
	s_sleep 8
	s_cbranch_scc0 .LBB0_187
	s_and_b64 vcc, exec, s[24:25]
	s_cbranch_vccz .LBB0_183

.LBB0_300:
	s_and_b32 s16, s10, 0xff
	s_mov_b64 s[14:15], -1
	s_cmp_lg_u32 s16, 0
	s_mov_b64 s[24:25], -1
	s_sleep 8
	s_cbranch_scc0 .LBB0_303
	s_and_b64 vcc, exec, s[24:25]
	s_cbranch_vccz .LBB0_299

.LBB0_319:
	s_and_b32 s23, s10, 0xff
	s_mov_b64 s[16:17], -1
	s_cmp_lg_u32 s23, 0
	s_mov_b64 s[26:27], -1
	s_sleep 8
	s_cbranch_scc0 .LBB0_322
	s_and_b64 vcc, exec, s[26:27]
	s_cbranch_vccz .LBB0_318
